# grid barrier leaders: early invalidate before TOPGEN spin, publish XCD generation before own invalidate
# speedup vs baseline: 1.0082x; 1.0034x over previous
; __device__ __forceinline__ unsigned xb_ld(unsigned* p)              { return __hip_atomic_load(p, __ATOMIC_RELAXED, __HIP_MEMORY_SCOPE_AGENT); }
; __device__ __forceinline__ unsigned xb_add(unsigned* p, unsigned v) { return __hip_atomic_fetch_add(p, v, __ATOMIC_RELAXED, __HIP_MEMORY_SCOPE_AGENT); }
; #define XB_SPIN(cond, bar) do { unsigned _sp = 0; while (cond) { __builtin_amdgcn_s_sleep(1); \
;     if ((++_sp & 255u) == 0u) { if (xb_ld(&(bar)[XB_TMO])) break; if (_sp > XB_SPIN_CAP) { atomicAdd(&(bar)[XB_TMO], 1u); break; } } } } while (0)
; __device__ __forceinline__ void xcd_barrier(const XcdBarrier& b) {
;     ...
;         const unsigned old = xb_add(&bar[XB_XSUB(b.x)], 1u);
;         const unsigned gen = old / nloc;
;         if (old + 1u == (gen + 1u) * nloc) {
;             __builtin_amdgcn_fence(__ATOMIC_RELEASE, "agent");
;             asm volatile("s_waitcnt vmcnt(0)" ::: "memory");
;             const unsigned og = xb_add(&bar[XB_TOP], 1u);
;             const unsigned tg = og / nx;
;             if (og + 1u == (tg + 1u) * nx) xb_add(&bar[XB_TOPGEN], 1u);
;             else XB_SPIN(xb_ld(&bar[XB_TOPGEN]) == tg, bar);
;             __builtin_amdgcn_fence(__ATOMIC_ACQUIRE, "agent");
;             xb_add(&bar[XB_XGEN(b.x)], 1u);
;             asm volatile("s_waitcnt vmcnt(0)" ::: "memory");
.LBB0_1012:
	s_or_b64 exec, exec, s[20:21]
	s_waitcnt vmcnt(0)
	v_readfirstlane_b32 s2, v4
	v_sub_u32_e32 v5, 0, v2
	s_mov_b64 s[20:21], -1
	v_add_u32_e32 v4, s2, v1
	v_cvt_f32_u32_e32 v1, v2
	v_readlane_b32 s2, v255, 27
	v_readlane_b32 s3, v255, 28
	v_rcp_iflag_f32_e32 v1, v1
	s_nop 0
	v_mul_f32_e32 v1, 0x4f7ffffe, v1
	v_cvt_u32_f32_e32 v1, v1
	v_mul_lo_u32 v5, v5, v1
	v_mul_hi_u32 v5, v1, v5
	v_add_u32_e32 v1, v1, v5
	v_mul_hi_u32 v1, v4, v1
	v_mul_lo_u32 v5, v1, v2
	v_sub_u32_e32 v5, v4, v5
	v_cmp_ge_u32_e32 vcc, v5, v2
	v_add_u32_e32 v6, 1, v1
	v_add_u32_e32 v4, 1, v4
	v_cndmask_b32_e32 v1, v1, v6, vcc
	v_sub_u32_e32 v6, v5, v2
	v_cndmask_b32_e32 v5, v5, v6, vcc
	v_cmp_ge_u32_e32 vcc, v5, v2
	v_add_u32_e32 v5, 1, v1
	s_nop 0
	v_cndmask_b32_e32 v1, v1, v5, vcc
	v_mul_lo_u32 v5, v2, v1
	v_add_u32_e32 v2, v5, v2
	v_cmp_ne_u32_e32 vcc, v4, v2
	v_mov_b64_e32 v[4:5], s[2:3]
	s_and_saveexec_b64 s[2:3], vcc
	s_cbranch_execz .LBB0_1024
	v_readlane_b32 s4, v255, 27
	v_readlane_b32 s5, v255, 28
	s_mov_b64 s[28:29], 0
	s_nop 3
	buffer_inv sc1
	global_load_dword v2, v3, s[4:5] sc1
	s_waitcnt vmcnt(0)
	v_cmp_eq_u32_e32 vcc, v2, v1
	s_and_saveexec_b64 s[20:21], vcc
	s_cbranch_execz .LBB0_1023
	s_mov_b32 s24, 1
	s_branch .LBB0_1016

; __device__ __forceinline__ unsigned xb_ld(unsigned* p)              { return __hip_atomic_load(p, __ATOMIC_RELAXED, __HIP_MEMORY_SCOPE_AGENT); }
; __device__ __forceinline__ unsigned xb_add(unsigned* p, unsigned v) { return __hip_atomic_fetch_add(p, v, __ATOMIC_RELAXED, __HIP_MEMORY_SCOPE_AGENT); }
; #define XB_SPIN(cond, bar) do { unsigned _sp = 0; while (cond) { __builtin_amdgcn_s_sleep(1); \
;     if ((++_sp & 255u) == 0u) { if (xb_ld(&(bar)[XB_TMO])) break; if (_sp > XB_SPIN_CAP) { atomicAdd(&(bar)[XB_TMO], 1u); break; } } } } while (0)
; __device__ __forceinline__ void xcd_barrier(const XcdBarrier& b) {
;     ...
;             const unsigned og = xb_add(&bar[XB_TOP], 1u);
;             const unsigned tg = og / nx;
;             if (og + 1u == (tg + 1u) * nx) xb_add(&bar[XB_TOPGEN], 1u);
;             else XB_SPIN(xb_ld(&bar[XB_TOPGEN]) == tg, bar);
;             __builtin_amdgcn_fence(__ATOMIC_ACQUIRE, "agent");
;             xb_add(&bar[XB_XGEN(b.x)], 1u);
;             asm volatile("s_waitcnt vmcnt(0)" ::: "memory");
.LBB0_1024:
	s_or_b64 exec, exec, s[2:3]
	s_mov_b32 s24, 0
	s_and_saveexec_b64 s[2:3], s[20:21]
	s_cbranch_execz .LBB0_1026
	s_mov_b32 s24, 1
	global_atomic_add v[4:5], v250, off
.LBB0_1026:
	s_or_b64 exec, exec, s[2:3]
	s_mov_b64 s[2:3], exec
	v_mbcnt_lo_u32_b32 v1, s2, 0
	v_mbcnt_hi_u32_b32 v1, s3, v1
	v_cmp_eq_u32_e32 vcc, 0, v1
	s_and_saveexec_b64 s[20:21], vcc
	s_cbranch_execz .LBB0_1028
	s_bcnt1_i32_b64 s2, s[2:3]
	v_mov_b32_e32 v1, s2
	v_readlane_b32 s2, v255, 23
	v_readlane_b32 s3, v255, 24
	s_nop 4
	global_atomic_add v3, v1, s[2:3]
.LBB0_1028:
	s_or_b64 exec, exec, s[20:21]
	s_cmp_eq_u32 s24, 0
	s_cbranch_scc1 .Lxb_noinv
	buffer_inv sc1
.Lxb_noinv:
	s_waitcnt vmcnt(0)
.LBB0_1029:
	s_or_b64 exec, exec, s[0:1]
	s_mov_b64 s[2:3], -1
	s_waitcnt lgkmcnt(0)
	s_barrier
